# speedup vs baseline: 1.0258x; 1.0258x over previous
.LBB0_11:
	s_and_b64 vcc, exec, s[4:5]
	s_cbranch_vccz .LBB0_20
	s_load_dwordx8 s[4:11], s[0:1], 0x8
	s_add_i32 s14, s2, 0xfffff800
	s_lshr_b32 s3, s14, 8
	s_bfe_u32 s13, s2, 0x40004
	s_and_b32 s12, s2, 15
	s_cmpk_lt_u32 s14, 0x100
	s_cselect_b64 vcc, -1, 0
	s_cmp_eq_u32 s3, 2
	s_waitcnt lgkmcnt(0)
	s_cselect_b32 s9, s9, s11
	s_cselect_b32 s8, s8, s10
	s_cmp_eq_u32 s3, 1
	s_cselect_b32 s8, s6, s8
	s_cselect_b32 s9, s7, s9
	s_and_b64 s[6:7], vcc, exec
	s_cselect_b32 s5, s5, s9
	s_cselect_b32 s4, s4, s8
	s_lshl_b32 s6, s12, 8
	s_add_u32 s4, s4, s6
	v_mov_b32_e32 v3, 0x3e38aa3b
	s_addc_u32 s5, s5, 0
	v_lshlrev_b32_e32 v8, 2, v2
	v_mov_b32_e32 v9, 0
	v_cndmask_b32_e32 v6, 1.0, v3, vcc
	v_lshl_add_u64 v[2:3], s[4:5], 0, v[8:9]
	s_lshl_b32 s4, s13, 18
	v_lshl_or_b32 v4, v1, 12, s4
	v_mov_b32_e32 v5, v9
	v_lshl_add_u64 v[10:11], v[2:3], 0, v[4:5]
	v_or_b32_e32 v5, 0x200, v0
	v_lshrrev_b32_e32 v13, 6, v5
	v_or_b32_e32 v5, 0x300, v0
	v_lshrrev_b32_e32 v28, 6, v5
	v_or_b32_e32 v5, 0x500, v0
	v_lshrrev_b32_e32 v29, 6, v5
	v_or_b32_e32 v5, 0x600, v0
	v_or_b32_e32 v12, 0x100, v0
	v_lshrrev_b32_e32 v30, 6, v5
	v_or_b32_e32 v5, 0x700, v0
	v_lshrrev_b32_e32 v7, 6, v12
	v_lshl_or_b32 v22, v29, 12, s4
	v_mov_b32_e32 v23, v9
	v_lshrrev_b32_e32 v31, 6, v5
	v_lshl_or_b32 v14, v7, 12, s4
	v_mov_b32_e32 v15, v9
	v_lshl_or_b32 v16, v13, 12, s4
	v_mov_b32_e32 v17, v9
	v_lshl_or_b32 v18, v28, 12, s4
	v_mov_b32_e32 v19, v9
	v_or_b32_e32 v20, 0x10000, v4
	v_mov_b32_e32 v21, v9
	v_lshl_add_u64 v[22:23], v[2:3], 0, v[22:23]
	v_lshl_or_b32 v24, v30, 12, s4
	v_mov_b32_e32 v25, v9
	v_lshl_or_b32 v26, v31, 12, s4
	v_mov_b32_e32 v27, v9
	v_or_b32_e32 v5, 0x900, v0
	v_lshl_add_u64 v[14:15], v[2:3], 0, v[14:15]
	v_lshl_add_u64 v[16:17], v[2:3], 0, v[16:17]
	v_lshl_add_u64 v[18:19], v[2:3], 0, v[18:19]
	v_lshl_add_u64 v[20:21], v[2:3], 0, v[20:21]
	v_lshl_add_u64 v[24:25], v[2:3], 0, v[24:25]
	v_lshl_add_u64 v[26:27], v[2:3], 0, v[26:27]
	global_load_dword v32, v[10:11], off nt
	global_load_dword v33, v[14:15], off nt
	global_load_dword v34, v[16:17], off nt
	global_load_dword v35, v[18:19], off nt
	global_load_dword v36, v[20:21], off nt
	global_load_dword v37, v[22:23], off nt
	global_load_dword v38, v[24:25], off nt
	global_load_dword v39, v[26:27], off nt
	v_or_b32_e32 v10, 0x20000, v4
	v_mov_b32_e32 v11, v9
	v_lshrrev_b32_e32 v23, 6, v5
	v_or_b32_e32 v5, 0xa00, v0
	v_lshl_add_u64 v[10:11], v[2:3], 0, v[10:11]
	v_lshrrev_b32_e32 v24, 6, v5
	v_or_b32_e32 v5, 0xb00, v0
	v_or_b32_e32 v18, 0xd00, v0
	v_or_b32_e32 v20, 0xe00, v0
	global_load_dword v22, v[10:11], off nt
	v_lshl_or_b32 v10, v23, 12, s4
	v_mov_b32_e32 v11, v9
	v_lshrrev_b32_e32 v25, 6, v5
	v_or_b32_e32 v4, 0x30000, v4
	v_mov_b32_e32 v5, v9
	v_lshrrev_b32_e32 v26, 6, v18
	v_lshrrev_b32_e32 v27, 6, v20
	v_lshl_add_u64 v[10:11], v[2:3], 0, v[10:11]
	v_lshl_or_b32 v14, v24, 12, s4
	v_mov_b32_e32 v15, v9
	v_lshl_or_b32 v16, v25, 12, s4
	v_mov_b32_e32 v17, v9
	v_lshl_add_u64 v[4:5], v[2:3], 0, v[4:5]
	v_lshl_or_b32 v18, v26, 12, s4
	v_mov_b32_e32 v19, v9
	v_lshl_or_b32 v20, v27, 12, s4
	v_mov_b32_e32 v21, v9
	v_lshl_add_u64 v[14:15], v[2:3], 0, v[14:15]
	v_lshl_add_u64 v[16:17], v[2:3], 0, v[16:17]
	v_lshl_add_u64 v[18:19], v[2:3], 0, v[18:19]
	v_lshl_add_u64 v[20:21], v[2:3], 0, v[20:21]
	global_load_dword v40, v[10:11], off nt
	global_load_dword v41, v[14:15], off nt
	global_load_dword v42, v[16:17], off nt
	global_load_dword v43, v[4:5], off nt
	global_load_dword v44, v[18:19], off nt
	global_load_dword v45, v[20:21], off nt
	v_or_b32_e32 v4, 0xf00, v0
	v_lshrrev_b32_e32 v10, 6, v4
	v_lshl_or_b32 v4, v10, 12, s4
	v_mov_b32_e32 v5, v9
	v_lshl_add_u64 v[2:3], v[2:3], 0, v[4:5]
	global_load_dword v2, v[2:3], off nt
	s_movk_i32 s8, 0x104
	v_mad_u32_u24 v1, v1, s8, v8
	v_mad_u32_u24 v3, v7, s8, v8
	s_cmpk_gt_u32 s14, 0x2ff
	v_lshrrev_b32_e32 v7, 3, v0
	s_movk_i32 s11, 0x820
	s_load_dwordx4 s[4:7], s[0:1], 0x38
	v_bfe_u32 v14, v0, 3, 2
	s_waitcnt vmcnt(15)
	ds_write_b32 v1, v32
	s_waitcnt vmcnt(14)
	ds_write_b32 v3, v33
	v_mad_u32_u24 v3, v13, s8, v8
	s_waitcnt vmcnt(13)
	ds_write_b32 v3, v34
	v_mad_u32_u24 v3, v28, s8, v8
	s_waitcnt vmcnt(12)
	ds_write_b32 v3, v35
	s_waitcnt vmcnt(11)
	ds_write_b32 v1, v36 offset:4160
	v_mad_u32_u24 v3, v29, s8, v8
	s_waitcnt vmcnt(10)
	ds_write_b32 v3, v37
	v_mad_u32_u24 v3, v30, s8, v8
	s_waitcnt vmcnt(9)
	ds_write_b32 v3, v38
	v_mad_u32_u24 v3, v31, s8, v8
	s_waitcnt vmcnt(8)
	ds_write_b32 v3, v39
	s_waitcnt vmcnt(7)
	ds_write_b32 v1, v22 offset:8320
	v_mad_u32_u24 v3, v23, s8, v8
	s_waitcnt vmcnt(6)
	ds_write_b32 v3, v40
	v_mad_u32_u24 v3, v24, s8, v8
	s_waitcnt vmcnt(5)
	ds_write_b32 v3, v41
	v_mad_u32_u24 v3, v25, s8, v8
	s_waitcnt vmcnt(4)
	ds_write_b32 v3, v42
	s_waitcnt vmcnt(3)
	ds_write_b32 v1, v43 offset:12480
	v_mad_u32_u24 v1, v26, s8, v8
	s_waitcnt vmcnt(2)
	ds_write_b32 v1, v44
	v_mad_u32_u24 v1, v27, s8, v8
	s_waitcnt vmcnt(1)
	ds_write_b32 v1, v45
	v_mad_u32_u24 v1, v10, s8, v8
	v_lshrrev_b32_e32 v3, 4, v0
	s_waitcnt vmcnt(0)
	ds_write_b32 v1, v2
	v_lshrrev_b32_e32 v2, 1, v0
	s_cselect_b64 s[8:9], -1, 0
	s_lshl_b32 s10, s12, 16
	v_and_b32_e32 v2, 16, v2
	v_and_b32_e32 v3, 12, v3
	s_mulk_i32 s12, 0xc0
	v_or3_b32 v2, v2, v3, s12
	v_and_b32_e32 v1, 7, v0
	v_lshl_add_u32 v13, s3, 5, v2
	v_lshlrev_b32_e32 v2, 2, v7
	v_mad_u32_u24 v4, v1, s11, v2
	s_waitcnt lgkmcnt(0)
	s_barrier
	ds_read2_b32 v[2:3], v4 offset1:65
	ds_read2_b32 v[16:17], v4 offset0:130 offset1:195
	v_add_u32_e32 v15, 0x400, v4
	ds_read2_b32 v[18:19], v15 offset0:4 offset1:69
	s_lshl_b32 s13, s13, 7
	s_waitcnt lgkmcnt(2)
	v_fma_mixlo_f16 v5, v6, v2, 0
	v_mov_b32_e32 v2, v3
	s_waitcnt lgkmcnt(1)
	v_mov_b32_e32 v3, v16
	v_mov_b32_e32 v4, v17
	ds_read2_b32 v[16:17], v15 offset0:134 offset1:199
	v_pk_mul_f32 v[2:3], v[6:7], v[2:3] op_sel_hi:[0,1]
	v_cvt_pk_f16_f32 v3, v2, v3
	v_pack_b32_f16 v2, v5, v3
	s_waitcnt lgkmcnt(1)
	v_mov_b32_e32 v5, v18
	v_pk_mul_f32 v[4:5], v[6:7], v[4:5] op_sel_hi:[0,1]
	v_cvt_pk_f16_f32 v15, v4, v5
	v_mov_b32_e32 v4, v19
	s_waitcnt lgkmcnt(0)
	v_mov_b32_e32 v5, v16
	s_add_u32 s6, s6, s13
	v_pk_mul_f32 v[4:5], v[6:7], v[4:5] op_sel_hi:[0,1]
	s_addc_u32 s7, s7, 0
	v_cvt_pk_f16_f32 v5, v4, v5
	v_lshlrev_b32_e32 v8, 4, v1
	s_add_u32 s4, s4, s13
	v_alignbit_b32 v4, v5, v15, 16
	v_lshrrev_b32_e32 v5, 16, v5
	v_lshl_add_u64 v[10:11], s[6:7], 0, v[8:9]
	s_addc_u32 s5, s5, 0
	v_alignbit_b32 v3, v15, v3, 16
	v_fma_mixhi_f16 v5, v6, v17, 0
	s_mov_b64 s[6:7], -1
	s_and_b64 vcc, exec, s[8:9]
	s_cbranch_vccz .LBB0_14
	v_lshlrev_b32_e32 v7, 10, v7
	v_add_lshl_u32 v16, v7, s10, 1
	v_mov_b32_e32 v17, v9
	v_lshl_add_u64 v[16:17], v[10:11], 0, v[16:17]
	global_store_dwordx4 v[16:17], v[2:5], off sc1
	s_mov_b64 s[6:7], 0
.LBB0_14:
	v_mul_u32_u24_e32 v15, 0x820, v1
	v_lshl_add_u64 v[8:9], s[4:5], 0, v[8:9]
	v_mov_b32_e32 v7, v6
	s_andn2_b64 vcc, exec, s[6:7]
	v_or_b32_e32 v1, v13, v14
	s_cbranch_vccnz .LBB0_16
	v_lshlrev_b32_e32 v16, 11, v1
	v_mov_b32_e32 v17, 0
	v_lshl_add_u64 v[16:17], v[8:9], 0, v[16:17]
	global_store_dwordx4 v[16:17], v[2:5], off sc1
.LBB0_16:
	v_lshrrev_b32_e32 v13, 3, v12
	s_nop 0
	v_lshl_add_u32 v4, v13, 2, v15
	ds_read2_b32 v[2:3], v4 offset1:65
	ds_read2_b32 v[16:17], v4 offset0:130 offset1:195
	v_add_u32_e32 v14, 0x400, v4
	ds_read2_b32 v[18:19], v14 offset0:4 offset1:69
	ds_read2_b32 v[14:15], v14 offset0:134 offset1:199
	s_waitcnt lgkmcnt(3)
	v_fma_mixlo_f16 v4, v6, v2, 0
	v_mov_b32_e32 v2, v3
	s_waitcnt lgkmcnt(2)
	v_mov_b32_e32 v3, v16
	v_pk_mul_f32 v[2:3], v[6:7], v[2:3]
	s_waitcnt lgkmcnt(1)
	v_mov_b32_e32 v5, v18
	v_cvt_pk_f16_f32 v3, v2, v3
	v_pack_b32_f16 v2, v4, v3
	v_mov_b32_e32 v4, v17
	v_pk_mul_f32 v[4:5], v[6:7], v[4:5]
	s_andn2_b64 vcc, exec, s[8:9]
	v_cvt_pk_f16_f32 v16, v4, v5
	v_mov_b32_e32 v4, v19
	s_waitcnt lgkmcnt(0)
	v_mov_b32_e32 v5, v14
	v_pk_mul_f32 v[4:5], v[6:7], v[4:5]
	v_alignbit_b32 v3, v16, v3, 16
	v_cvt_pk_f16_f32 v5, v4, v5
	v_alignbit_b32 v4, v5, v16, 16
	v_lshrrev_b32_e32 v5, 16, v5
	v_fma_mixhi_f16 v5, v6, v15, 0
	s_mov_b64 s[4:5], -1
	s_cbranch_vccnz .LBB0_18
	v_lshlrev_b32_e32 v6, 10, v13
	v_add_lshl_u32 v6, v6, s10, 1
	v_mov_b32_e32 v7, 0
	v_lshl_add_u64 v[6:7], v[10:11], 0, v[6:7]
	s_mov_b64 s[4:5], 0
	global_store_dwordx4 v[6:7], v[2:5], off sc1
.LBB0_18:
	s_andn2_b64 vcc, exec, s[4:5]
	s_cbranch_vccnz .LBB0_20
	v_lshrrev_b32_e32 v6, 8, v12
	v_mul_u32_u24_e32 v6, 0x60, v6
	v_add_lshl_u32 v6, v1, v6, 11
	v_mov_b32_e32 v7, 0
	v_lshl_add_u64 v[6:7], v[8:9], 0, v[6:7]
	global_store_dwordx4 v[6:7], v[2:5], off sc1

.LBB0_23:
	s_load_dwordx2 s[4:5], s[0:1], 0x0
	s_load_dwordx2 s[6:7], s[0:1], 0x30
	s_ashr_i32 s3, s2, 31
	s_lshl_b64 s[0:1], s[2:3], 11
	v_lshl_or_b32 v8, v0, 3, s0
	v_mov_b32_e32 v9, s1
	s_waitcnt lgkmcnt(0)
	v_lshl_add_u64 v[10:11], v[8:9], 2, s[4:5]
	global_load_dwordx4 v[0:3], v[10:11], off offset:16 nt
	global_load_dwordx4 v[4:7], v[10:11], off nt
	s_waitcnt vmcnt(1)
	v_cvt_pk_f16_f32 v3, v2, v3
	v_cvt_pk_f16_f32 v2, v0, v1
	s_waitcnt vmcnt(0)
	v_cvt_pk_f16_f32 v1, v6, v7
	v_cvt_pk_f16_f32 v0, v4, v5
	v_lshl_add_u64 v[4:5], v[8:9], 1, s[6:7]
	global_store_dwordx4 v[4:5], v[0:3], off sc1
	s_endpgm

.LBB1_47:
	v_div_scale_f32 v0, s[0:1], v74, v74, 1.0
	v_rcp_f32_e32 v1, v0
	v_div_scale_f32 v2, vcc, 1.0, v74, 1.0
	s_lshl_b32 s0, s3, 7
	v_fma_f32 v3, -v0, v1, 1.0
	v_fmac_f32_e32 v1, v3, v1
	v_mul_f32_e32 v3, v2, v1
	v_fma_f32 v4, -v0, v3, v2
	v_fmac_f32_e32 v3, v4, v1
	v_fma_f32 v0, -v0, v3, v2
	v_div_fmas_f32 v0, v0, v1, v3
	s_and_b32 s0, s0, 0x800
	v_div_fixup_f32 v4, v0, v74, 1.0
	v_add_u32_e32 v0, s0, v86
	v_ashrrev_i32_e32 v1, 31, v0
	v_lshlrev_b64 v[0:1], 11, v[0:1]
	s_lshl_b32 s0, s2, 7
	v_lshl_add_u64 v[0:1], s[20:21], 0, v[0:1]
	s_and_b32 s0, s0, 0x780
	s_mov_b32 s1, 0
	v_lshl_add_u64 v[0:1], v[0:1], 0, s[0:1]
	v_lshlrev_b32_e32 v2, 1, v88
	v_mov_b32_e32 v3, 0
	v_lshl_add_u64 v[6:7], v[0:1], 0, v[2:3]
	v_mov_b32_e32 v0, v71
	v_mov_b32_e32 v1, v72
	v_pk_mul_f32 v[0:1], v[4:5], v[0:1] op_sel_hi:[0,1]
	v_fma_mixlo_f16 v2, v4, v70, 0
	v_cvt_pk_f16_f32 v1, v0, v1
	v_pack_b32_f16 v0, v2, v1
	v_mov_b32_e32 v2, v67
	v_mov_b32_e32 v3, v68
	v_pk_mul_f32 v[2:3], v[4:5], v[2:3] op_sel_hi:[0,1]
	v_cvt_pk_f16_f32 v5, v2, v3
	v_pk_mov_b32 v[2:3], v[72:73], v[66:67] op_sel:[1,0]
	s_nop 0
	v_pk_mul_f32 v[2:3], v[4:5], v[2:3] op_sel_hi:[0,1]
	v_cvt_pk_f16_f32 v2, v2, v3
	v_lshrrev_b32_e32 v3, 16, v5
	v_alignbit_b32 v1, v2, v1, 16
	v_alignbit_b32 v2, v5, v2, 16
	v_fma_mixhi_f16 v3, v4, v69, 0
	global_store_dwordx4 v[6:7], v[0:3], off sc1
	s_nop 1
	v_mov_b32_e32 v0, v63
	v_mov_b32_e32 v1, v64
	v_pk_mul_f32 v[0:1], v[4:5], v[0:1] op_sel_hi:[0,1]
	v_fma_mixlo_f16 v2, v4, v62, 0
	v_cvt_pk_f16_f32 v1, v0, v1
	v_pack_b32_f16 v0, v2, v1
	v_mov_b32_e32 v2, v59
	v_mov_b32_e32 v3, v60
	v_pk_mul_f32 v[2:3], v[4:5], v[2:3] op_sel_hi:[0,1]
	v_cvt_pk_f16_f32 v5, v2, v3
	v_pk_mov_b32 v[2:3], v[64:65], v[58:59] op_sel:[1,0]
	s_nop 0
	v_pk_mul_f32 v[2:3], v[4:5], v[2:3] op_sel_hi:[0,1]
	v_cvt_pk_f16_f32 v2, v2, v3
	v_lshrrev_b32_e32 v3, 16, v5
	v_alignbit_b32 v1, v2, v1, 16
	v_alignbit_b32 v2, v5, v2, 16
	v_fma_mixhi_f16 v3, v4, v61, 0
	global_store_dwordx4 v[6:7], v[0:3], off offset:64 sc1

.LBB2_1:
	s_mul_i32 s22, s21, 0xe000
	v_add_u32_e32 v166, s22, v146
	v_add_u32_e32 v190, s22, v153
	s_waitcnt lgkmcnt(0)
	v_mfma_f32_16x16x32_f16 v[130:133], v[22:25], v[42:45], v[130:133]
	ds_read_b128 v[154:157], v166 offset:1024
	ds_read_b128 v[158:161], v166 offset:3072
	s_add_i32 s21, s21, 1
	v_mfma_f32_16x16x32_f16 v[98:101], v[18:21], v[42:45], v[98:101]
	ds_read_b128 v[162:165], v166 offset:5120
	ds_read_b128 v[166:169], v166 offset:7168
	v_mfma_f32_16x16x32_f16 v[86:89], v[30:33], v[42:45], v[86:89]
	ds_read_b128 v[170:173], v190 offset:33792
	ds_read_b128 v[174:177], v190 offset:35840
	v_mfma_f32_16x16x32_f16 v[74:77], v[26:29], v[42:45], v[74:77]
	ds_read_b128 v[178:181], v190 offset:37888
	ds_read_b128 v[182:185], v190 offset:39936
	v_mfma_f32_16x16x32_f16 v[70:73], v[42:45], v[34:37], v[70:73]
	ds_read_b128 v[186:189], v190 offset:41984
	ds_read_b128 v[190:193], v190 offset:44032
	v_mfma_f32_16x16x32_f16 v[66:69], v[42:45], v[14:17], v[66:69]
	v_mfma_f32_16x16x32_f16 v[62:65], v[22:25], v[38:41], v[62:65]
	v_mfma_f32_16x16x32_f16 v[58:61], v[18:21], v[38:41], v[58:61]
	v_mfma_f32_16x16x32_f16 v[54:57], v[30:33], v[38:41], v[54:57]
	v_mfma_f32_16x16x32_f16 v[50:53], v[26:29], v[38:41], v[50:53]
	v_mfma_f32_16x16x32_f16 v[46:49], v[38:41], v[34:37], v[46:49]
	v_mfma_f32_16x16x32_f16 v[2:5], v[38:41], v[14:17], v[2:5]
	v_mfma_f32_16x16x32_f16 v[78:81], v[22:25], v[10:13], v[78:81]
	v_mfma_f32_16x16x32_f16 v[82:85], v[18:21], v[10:13], v[82:85]
	v_mfma_f32_16x16x32_f16 v[90:93], v[30:33], v[10:13], v[90:93]
	v_mfma_f32_16x16x32_f16 v[94:97], v[26:29], v[10:13], v[94:97]
	v_mfma_f32_16x16x32_f16 v[102:105], v[10:13], v[34:37], v[102:105]
	v_mfma_f32_16x16x32_f16 v[106:109], v[10:13], v[14:17], v[106:109]
	v_mfma_f32_16x16x32_f16 v[110:113], v[22:25], v[6:9], v[110:113]
	v_mfma_f32_16x16x32_f16 v[114:117], v[18:21], v[6:9], v[114:117]
	v_mfma_f32_16x16x32_f16 v[118:121], v[30:33], v[6:9], v[118:121]
	v_mfma_f32_16x16x32_f16 v[122:125], v[26:29], v[6:9], v[122:125]
	v_mfma_f32_16x16x32_f16 v[134:137], v[6:9], v[34:37], v[134:137]
	v_mfma_f32_16x16x32_f16 v[126:129], v[6:9], v[14:17], v[126:129]
	v_or_b32_e32 v10, s22, v139
	v_lshl_add_u64 v[6:7], v[142:143], 0, s[0:1]
	v_readfirstlane_b32 s22, v10
	v_add_u32_e32 v11, 0x2000, v10
	v_lshl_add_u64 v[8:9], v[6:7], 0, s[2:3]
	s_mov_b32 m0, s22
	v_readfirstlane_b32 s22, v11
	v_add_u32_e32 v11, 0x4000, v10
	s_waitcnt vmcnt(0) lgkmcnt(0)
	s_barrier
	global_load_lds_dwordx4 v[8:9], off
	v_lshl_add_u64 v[8:9], v[6:7], 0, s[8:9]
	s_mov_b32 m0, s22
	v_readfirstlane_b32 s22, v11
	global_load_lds_dwordx4 v[8:9], off
	v_lshl_add_u64 v[8:9], v[6:7], 0, s[16:17]
	s_mov_b32 m0, s22
	v_lshl_add_u64 v[6:7], v[6:7], 0, s[18:19]
	global_load_lds_dwordx4 v[8:9], off
	v_add_u32_e32 v8, 0x6000, v10
	v_add_u32_e32 v11, 0x8000, v10
	v_readfirstlane_b32 s22, v8
	s_mov_b32 m0, s22
	v_readfirstlane_b32 s22, v11
	global_load_lds_dwordx4 v[6:7], off
	v_lshl_add_u64 v[6:7], v[140:141], 0, s[0:1]
	v_add_u32_e32 v11, 0xa000, v10
	v_lshl_add_u64 v[8:9], v[6:7], 0, s[2:3]
	s_mov_b32 m0, s22
	v_readfirstlane_b32 s22, v11
	global_load_lds_dwordx4 v[8:9], off
	v_lshl_add_u64 v[8:9], v[6:7], 0, s[8:9]
	s_mov_b32 m0, s22
	v_lshl_add_u64 v[6:7], v[6:7], 0, s[16:17]
	global_load_lds_dwordx4 v[8:9], off
	v_add_u32_e32 v8, 0xc000, v10
	s_cmp_lg_u32 s21, 2
	v_readfirstlane_b32 s22, v8
	s_mov_b32 m0, s22
	s_cselect_b32 s21, s21, 0
	global_load_lds_dwordx4 v[6:7], off
	s_mul_i32 s22, s21, 0xe000
	v_add_u32_e32 v6, s22, v146
	v_add_u32_e32 v14, s22, v153
	s_waitcnt lgkmcnt(0)
	v_mfma_f32_16x16x32_f16 v[130:133], v[170:173], v[154:157], v[130:133]
	ds_read_b128 v[42:45], v6
	ds_read_b128 v[38:41], v6 offset:2048
	v_mfma_f32_16x16x32_f16 v[98:101], v[174:177], v[154:157], v[98:101]
	ds_read_b128 v[10:13], v6 offset:4096
	ds_read_b128 v[6:9], v6 offset:6144
	v_mfma_f32_16x16x32_f16 v[86:89], v[178:181], v[154:157], v[86:89]
	ds_read_b128 v[22:25], v14 offset:32768
	ds_read_b128 v[18:21], v14 offset:34816
	v_mfma_f32_16x16x32_f16 v[74:77], v[182:185], v[154:157], v[74:77]
	ds_read_b128 v[30:33], v14 offset:36864
	ds_read_b128 v[26:29], v14 offset:38912
	v_mfma_f32_16x16x32_f16 v[70:73], v[154:157], v[186:189], v[70:73]
	ds_read_b128 v[34:37], v14 offset:40960
	ds_read_b128 v[14:17], v14 offset:43008
	v_mfma_f32_16x16x32_f16 v[66:69], v[154:157], v[190:193], v[66:69]
	v_mfma_f32_16x16x32_f16 v[62:65], v[170:173], v[158:161], v[62:65]
	v_mfma_f32_16x16x32_f16 v[58:61], v[174:177], v[158:161], v[58:61]
	v_mfma_f32_16x16x32_f16 v[54:57], v[178:181], v[158:161], v[54:57]
	v_mfma_f32_16x16x32_f16 v[50:53], v[182:185], v[158:161], v[50:53]
	v_mfma_f32_16x16x32_f16 v[46:49], v[158:161], v[186:189], v[46:49]
	v_mfma_f32_16x16x32_f16 v[2:5], v[158:161], v[190:193], v[2:5]
	v_mfma_f32_16x16x32_f16 v[78:81], v[170:173], v[162:165], v[78:81]
	v_mfma_f32_16x16x32_f16 v[82:85], v[174:177], v[162:165], v[82:85]
	v_mfma_f32_16x16x32_f16 v[90:93], v[178:181], v[162:165], v[90:93]
	v_mfma_f32_16x16x32_f16 v[94:97], v[182:185], v[162:165], v[94:97]
	v_mfma_f32_16x16x32_f16 v[102:105], v[162:165], v[186:189], v[102:105]
	v_mfma_f32_16x16x32_f16 v[106:109], v[162:165], v[190:193], v[106:109]
	v_mfma_f32_16x16x32_f16 v[110:113], v[170:173], v[166:169], v[110:113]
	v_mfma_f32_16x16x32_f16 v[114:117], v[174:177], v[166:169], v[114:117]
	v_mfma_f32_16x16x32_f16 v[118:121], v[178:181], v[166:169], v[118:121]
	v_mfma_f32_16x16x32_f16 v[122:125], v[182:185], v[166:169], v[122:125]
	v_mfma_f32_16x16x32_f16 v[134:137], v[166:169], v[186:189], v[134:137]
	v_mfma_f32_16x16x32_f16 v[126:129], v[166:169], v[190:193], v[126:129]
	s_add_u32 s0, s0, 0x80
	s_addc_u32 s1, s1, 0
	s_cmpk_eq_i32 s0, 0x700
	s_cbranch_scc0 .LBB2_1
	s_waitcnt lgkmcnt(0)
	v_mfma_f32_16x16x32_f16 v[130:133], v[22:25], v[42:45], v[130:133]
	ds_read_b128 v[140:143], v146 offset:1024
	ds_read_b128 v[154:157], v146 offset:3072
	v_mfma_f32_16x16x32_f16 v[98:101], v[18:21], v[42:45], v[98:101]
	ds_read_b128 v[158:161], v146 offset:5120
	ds_read_b128 v[162:165], v146 offset:7168
	v_mfma_f32_16x16x32_f16 v[86:89], v[30:33], v[42:45], v[86:89]
	ds_read_b128 v[166:169], v153 offset:33792
	ds_read_b128 v[170:173], v153 offset:35840
	v_mfma_f32_16x16x32_f16 v[74:77], v[26:29], v[42:45], v[74:77]
	ds_read_b128 v[174:177], v153 offset:37888
	ds_read_b128 v[178:181], v153 offset:39936
	v_mfma_f32_16x16x32_f16 v[70:73], v[42:45], v[34:37], v[70:73]
	ds_read_b128 v[182:185], v153 offset:41984
	ds_read_b128 v[186:189], v153 offset:44032
	v_mfma_f32_16x16x32_f16 v[42:45], v[42:45], v[14:17], v[66:69]
	v_mfma_f32_16x16x32_f16 v[62:65], v[22:25], v[38:41], v[62:65]
	v_mfma_f32_16x16x32_f16 v[58:61], v[18:21], v[38:41], v[58:61]
	v_mfma_f32_16x16x32_f16 v[54:57], v[30:33], v[38:41], v[54:57]
	v_mfma_f32_16x16x32_f16 v[50:53], v[26:29], v[38:41], v[50:53]
	v_mfma_f32_16x16x32_f16 v[46:49], v[38:41], v[34:37], v[46:49]
	v_mfma_f32_16x16x32_f16 v[2:5], v[38:41], v[14:17], v[2:5]
	v_mfma_f32_16x16x32_f16 v[38:41], v[22:25], v[10:13], v[78:81]
	v_mfma_f32_16x16x32_f16 v[66:69], v[18:21], v[10:13], v[82:85]
	v_mfma_f32_16x16x32_f16 v[78:81], v[30:33], v[10:13], v[90:93]
	v_mfma_f32_16x16x32_f16 v[82:85], v[26:29], v[10:13], v[94:97]
	v_mfma_f32_16x16x32_f16 v[90:93], v[10:13], v[34:37], v[102:105]
	v_mfma_f32_16x16x32_f16 v[94:97], v[10:13], v[14:17], v[106:109]
	v_mfma_f32_16x16x32_f16 v[22:25], v[22:25], v[6:9], v[110:113]
	v_mfma_f32_16x16x32_f16 v[102:105], v[18:21], v[6:9], v[114:117]
	v_or_b32_e32 v21, v151, v152
	v_and_b32_e32 v20, 63, v0
	v_mfma_f32_16x16x32_f16 v[30:33], v[30:33], v[6:9], v[118:121]
	v_mfma_f32_16x16x32_f16 v[26:29], v[26:29], v[6:9], v[122:125]
	v_mfma_f32_16x16x32_f16 v[34:37], v[6:9], v[34:37], v[134:137]
	v_mfma_f32_16x16x32_f16 v[6:9], v[6:9], v[14:17], v[126:129]
	v_add_u32_e32 v10, 0x16800, v21
	s_waitcnt vmcnt(0) lgkmcnt(0)
	s_waitcnt lgkmcnt(0)
	v_mfma_f32_16x16x32_f16 v[16:19], v[166:169], v[140:143], v[130:133]
	s_barrier
	ds_read_b128 v[106:109], v146 offset:57344
	ds_read_b128 v[110:113], v146 offset:59392
	v_mfma_f32_16x16x32_f16 v[98:101], v[170:173], v[140:143], v[98:101]
	ds_read_b128 v[114:117], v146 offset:61440
	ds_read_b128 v[12:15], v146 offset:63488
	v_add_u32_e32 v0, 0x16000, v21
	v_mfma_f32_16x16x32_f16 v[86:89], v[174:177], v[140:143], v[86:89]
	ds_read_b128 v[122:125], v10
	v_add_u32_e32 v10, 0x17000, v21
	ds_read_b128 v[118:121], v0
	v_mfma_f32_16x16x32_f16 v[74:77], v[178:181], v[140:143], v[74:77]
	ds_read_b128 v[126:129], v10
	v_add_u32_e32 v10, 0x17800, v21
	ds_read_b128 v[130:133], v10
	v_mfma_f32_16x16x32_f16 v[70:73], v[140:143], v[182:185], v[70:73]
	ds_read_b128 v[134:137], v0 offset:8192
	ds_read_b128 v[190:193], v0 offset:10240
	v_mfma_f32_16x16x32_f16 v[42:45], v[140:143], v[186:189], v[42:45]
	v_mfma_f32_16x16x32_f16 v[62:65], v[166:169], v[154:157], v[62:65]
	v_mfma_f32_16x16x32_f16 v[58:61], v[170:173], v[154:157], v[58:61]
	v_mfma_f32_16x16x32_f16 v[54:57], v[174:177], v[154:157], v[54:57]
	v_mfma_f32_16x16x32_f16 v[50:53], v[178:181], v[154:157], v[50:53]
	v_mfma_f32_16x16x32_f16 v[46:49], v[154:157], v[182:185], v[46:49]
	v_mfma_f32_16x16x32_f16 v[140:143], v[154:157], v[186:189], v[2:5]
	v_mfma_f32_16x16x32_f16 v[38:41], v[166:169], v[158:161], v[38:41]
	v_mfma_f32_16x16x32_f16 v[66:69], v[170:173], v[158:161], v[66:69]
	v_mfma_f32_16x16x32_f16 v[78:81], v[174:177], v[158:161], v[78:81]
	v_mfma_f32_16x16x32_f16 v[82:85], v[178:181], v[158:161], v[82:85]
	v_mfma_f32_16x16x32_f16 v[90:93], v[158:161], v[182:185], v[90:93]
	v_mfma_f32_16x16x32_f16 v[94:97], v[158:161], v[186:189], v[94:97]
	v_mfma_f32_16x16x32_f16 v[22:25], v[166:169], v[162:165], v[22:25]
	v_mfma_f32_16x16x32_f16 v[102:105], v[170:173], v[162:165], v[102:105]
	v_mfma_f32_16x16x32_f16 v[30:33], v[174:177], v[162:165], v[30:33]
	v_mfma_f32_16x16x32_f16 v[26:29], v[178:181], v[162:165], v[26:29]
	v_mfma_f32_16x16x32_f16 v[34:37], v[162:165], v[182:185], v[34:37]
	v_mfma_f32_16x16x32_f16 v[152:155], v[162:165], v[186:189], v[6:9]
	s_waitcnt lgkmcnt(0)
	v_mfma_f32_16x16x32_f16 v[156:159], v[118:121], v[106:109], v[16:19]
	s_movk_i32 s0, 0x7c0
	ds_read_b128 v[202:205], v0 offset:9216
	ds_read_b128 v[206:209], v0 offset:11264
	v_lshlrev_b32_e32 v16, 6, v144
	v_mov_b32_e32 v17, 0
	v_mov_b32_e32 v139, v17
	v_lshl_add_u64 v[4:5], s[6:7], 0, v[16:17]
	v_lshl_add_u64 v[8:9], v[4:5], 0, v[138:139]
	s_waitcnt vmcnt(0)
	v_lshlrev_b32_e32 v4, 5, v150
	v_lshl_add_u64 v[2:3], s[4:5], 0, v[16:17]
	v_ashrrev_i32_e32 v5, 31, v4
	v_lshl_add_u64 v[2:3], v[2:3], 0, v[138:139]
	v_lshlrev_b64 v[4:5], 2, v[4:5]
	v_lshl_add_u64 v[6:7], v[2:3], 0, v[4:5]
	v_lshl_add_u64 v[4:5], v[8:9], 0, v[4:5]
	v_mfma_f32_16x16x32_f16 v[98:101], v[122:125], v[106:109], v[98:101]
	global_load_dwordx4 v[160:163], v[6:7], off
	v_lshlrev_b32_e32 v18, 5, v147
	v_ashrrev_i32_e32 v19, 31, v18
	v_mfma_f32_16x16x32_f16 v[86:89], v[126:129], v[106:109], v[86:89]
	v_lshlrev_b64 v[18:19], 2, v[18:19]
	ds_read_b128 v[172:175], v146 offset:62464
	ds_read_b128 v[176:179], v146 offset:64512
	v_mfma_f32_16x16x32_f16 v[74:77], v[130:133], v[106:109], v[74:77]
	v_mfma_f32_16x16x32_f16 v[70:73], v[106:109], v[134:137], v[70:73]
	v_mfma_f32_16x16x32_f16 v[42:45], v[106:109], v[190:193], v[42:45]
	global_load_dwordx4 v[106:109], v[4:5], off
	v_lshlrev_b32_e32 v4, 5, v149
	v_ashrrev_i32_e32 v5, 31, v4
	v_lshlrev_b64 v[4:5], 2, v[4:5]
	v_lshl_add_u64 v[6:7], v[2:3], 0, v[4:5]
	v_lshl_add_u64 v[4:5], v[8:9], 0, v[4:5]
	global_load_dwordx4 v[168:171], v[4:5], off
	global_load_dwordx4 v[164:167], v[6:7], off
	v_lshlrev_b32_e32 v4, 5, v148
	v_ashrrev_i32_e32 v5, 31, v4
	v_lshlrev_b64 v[10:11], 2, v[4:5]
	v_lshl_add_u64 v[4:5], v[2:3], 0, v[10:11]
	v_lshl_add_u64 v[10:11], v[8:9], 0, v[10:11]
	global_load_dwordx4 v[210:213], v[10:11], off
	v_lshl_add_u64 v[2:3], v[2:3], 0, v[18:19]
	global_load_dwordx4 v[4:7], v[4:5], off
	v_lshl_add_u64 v[8:9], v[8:9], 0, v[18:19]
	v_add_u32_e32 v18, 0x16400, v21
	v_ashrrev_i32_e32 v10, 7, v145
	ds_read_b128 v[180:183], v18
	v_add_u32_e32 v18, 0x17400, v21
	v_and_b32_e32 v10, -16, v10
	v_add_u32_e32 v19, 0x16c00, v21
	ds_read_b128 v[194:197], v18
	v_add_u32_e32 v18, s20, v10
	global_load_dwordx4 v[8:11], v[8:9], off
	ds_read_b128 v[184:187], v19
	v_add_u32_e32 v19, 0x17c00, v21
	v_and_or_b32 v21, v145, s0, v1
	global_load_dwordx4 v[0:3], v[2:3], off
	v_mfma_f32_16x16x32_f16 v[62:65], v[118:121], v[110:113], v[62:65]
	ds_read_b128 v[198:201], v19
	v_ashrrev_i32_e32 v19, 31, v18
	ds_read_b128 v[148:151], v146 offset:60416
	v_mfma_f32_16x16x32_f16 v[58:61], v[122:125], v[110:113], v[58:61]
	v_mfma_f32_16x16x32_f16 v[54:57], v[126:129], v[110:113], v[54:57]
	v_mfma_f32_16x16x32_f16 v[50:53], v[130:133], v[110:113], v[50:53]
	v_mfma_f32_16x16x32_f16 v[46:49], v[110:113], v[134:137], v[46:49]
	v_mfma_f32_16x16x32_f16 v[110:113], v[110:113], v[190:193], v[140:143]
	s_nop 2
	ds_read_b128 v[140:143], v146 offset:58368
	v_mfma_f32_16x16x32_f16 v[38:41], v[118:121], v[114:117], v[38:41]
	v_mfma_f32_16x16x32_f16 v[66:69], v[122:125], v[114:117], v[66:69]
	v_mfma_f32_16x16x32_f16 v[78:81], v[126:129], v[114:117], v[78:81]
	v_mfma_f32_16x16x32_f16 v[82:85], v[130:133], v[114:117], v[82:85]
	v_mfma_f32_16x16x32_f16 v[90:93], v[114:117], v[134:137], v[90:93]
	v_mfma_f32_16x16x32_f16 v[94:97], v[114:117], v[190:193], v[94:97]
	s_waitcnt lgkmcnt(0)
	v_mfma_f32_16x16x32_f16 v[114:117], v[180:183], v[140:143], v[156:159]
	v_mfma_f32_16x16x32_f16 v[98:101], v[184:187], v[140:143], v[98:101]
	v_mfma_f32_16x16x32_f16 v[22:25], v[118:121], v[12:15], v[22:25]
	s_waitcnt vmcnt(6)
	s_nop 4
	v_pk_mul_f32 v[120:121], v[114:115], v[106:107] op_sel_hi:[1,0]
	v_lshlrev_b64 v[118:119], 17, v[18:19]
	v_lshl_or_b32 v118, v21, 6, v118
	v_mfma_f32_16x16x32_f16 v[102:105], v[122:125], v[12:15], v[102:105]
	v_mul_f32_e64 v122, v116, v107
	v_mul_f32_e64 v123, v117, v107
	v_pk_fma_f32 v[124:125], v[114:115], v[160:161], v[120:121] op_sel:[0,0,1] op_sel_hi:[1,1,0] neg_lo:[0,0,1] neg_hi:[0,0,1]
	v_pk_fma_f32 v[114:115], v[114:115], v[160:161], v[120:121] op_sel:[0,0,1] op_sel_hi:[1,0,0]
	v_pk_fma_f32 v[120:121], v[116:117], v[160:161], v[122:123] op_sel:[0,1,1] op_sel_hi:[1,1,0] neg_lo:[0,0,1] neg_hi:[0,0,1]
	v_pk_fma_f32 v[116:117], v[116:117], v[160:161], v[122:123] op_sel:[0,1,1] op_sel_hi:[1,1,0]
	v_cvt_pk_f16_f32 v114, v124, v115
	v_cvt_pk_f16_f32 v115, v120, v117
	v_pk_mul_f32 v[116:117], v[98:99], v[108:109] op_sel_hi:[1,0]
	v_mov_b32_e32 v122, v163
	v_pk_fma_f32 v[120:121], v[98:99], v[162:163], v[116:117] op_sel:[0,0,1] op_sel_hi:[1,1,0] neg_lo:[0,0,1] neg_hi:[0,0,1]
	v_pk_fma_f32 v[98:99], v[98:99], v[162:163], v[116:117] op_sel:[0,0,1] op_sel_hi:[1,0,0]
	v_mfma_f32_16x16x32_f16 v[30:33], v[126:129], v[12:15], v[30:33]
	v_cvt_pk_f16_f32 v116, v120, v99
	v_mov_b32_e32 v120, v109
	v_pk_mul_f32 v[98:99], v[100:101], v[120:121] op_sel_hi:[1,0]
	v_mfma_f32_16x16x32_f16 v[26:29], v[130:133], v[12:15], v[26:29]
	v_fma_f32 v124, v100, v122, -v99
	v_fma_f32 v125, v101, v122, -v98
	v_pk_fma_f32 v[98:99], v[100:101], v[122:123], v[98:99] op_sel:[0,0,1] op_sel_hi:[1,0,0]
	s_nop 0
	v_cvt_pk_f16_f32 v117, v124, v99
	v_lshlrev_b64 v[124:125], 1, v[118:119]
	v_lshl_add_u64 v[126:127], s[10:11], 0, v[124:125]
	v_mfma_f32_16x16x32_f16 v[34:37], v[12:15], v[134:137], v[34:37]
	v_mfma_f32_16x16x32_f16 v[98:101], v[12:15], v[190:193], v[152:155]
	v_lshl_add_u64 v[12:13], v[126:127], 0, v[16:17]
	v_lshl_add_u64 v[126:127], v[12:13], 0, v[138:139]
	global_store_dwordx4 v[126:127], v[114:117], off sc1
	v_mfma_f32_16x16x32_f16 v[12:15], v[194:197], v[140:143], v[86:89]
	v_mfma_f32_16x16x32_f16 v[74:77], v[198:201], v[140:143], v[74:77]
	v_mfma_f32_16x16x32_f16 v[58:61], v[184:187], v[148:151], v[58:61]
	s_nop 5
	v_mul_f32_e64 v86, v12, v106
	v_mul_f32_e64 v87, v13, v106
	v_pk_fma_f32 v[88:89], v[12:13], v[160:161], v[86:87] op_sel:[0,0,1] op_sel_hi:[1,1,0] neg_lo:[0,0,1] neg_hi:[0,0,1]
	v_pk_fma_f32 v[12:13], v[12:13], v[160:161], v[86:87] op_sel:[0,0,1] op_sel_hi:[1,0,0]
	v_mfma_f32_16x16x32_f16 v[54:57], v[194:197], v[148:151], v[54:57]
	v_cvt_pk_f16_f32 v86, v88, v13
	v_pk_mul_f32 v[12:13], v[14:15], v[106:107] op_sel:[0,1]
	s_nop 0
	v_pk_fma_f32 v[88:89], v[14:15], v[160:161], v[12:13] op_sel:[0,1,1] op_sel_hi:[1,1,0] neg_lo:[0,0,1] neg_hi:[0,0,1]
	v_pk_fma_f32 v[12:13], v[14:15], v[160:161], v[12:13] op_sel:[0,1,1] op_sel_hi:[1,1,0]
	v_mfma_f32_16x16x32_f16 v[50:53], v[198:201], v[148:151], v[50:53]
	v_cvt_pk_f16_f32 v87, v88, v13
	v_pk_mul_f32 v[88:89], v[74:75], v[108:109] op_sel_hi:[1,0]
	v_mfma_f32_16x16x32_f16 v[12:15], v[140:143], v[206:209], v[42:45]
	s_nop 2
	v_fma_f32 v42, v74, v162, -v89
	v_fma_f32 v43, v75, v163, -v88
	v_pk_fma_f32 v[44:45], v[74:75], v[162:163], v[88:89] op_sel:[0,0,1] op_sel_hi:[1,0,0]
	v_mfma_f32_16x16x32_f16 v[38:41], v[180:183], v[172:175], v[38:41]
	v_cvt_pk_f16_f32 v88, v42, v45
	v_mfma_f32_16x16x32_f16 v[42:45], v[180:183], v[148:151], v[62:65]
	s_nop 2
	v_mul_f32_e64 v62, v76, v120
	v_mul_f32_e64 v63, v77, v120
	v_mfma_f32_16x16x32_f16 v[66:69], v[184:187], v[172:175], v[66:69]
	v_fma_f32 v64, v76, v122, -v63
	v_fma_f32 v65, v77, v122, -v62
	v_pk_fma_f32 v[62:63], v[76:77], v[122:123], v[62:63] op_sel:[0,0,1] op_sel_hi:[1,0,0]
	s_nop 0
	v_cvt_pk_f16_f32 v89, v64, v63
	v_lshl_add_u64 v[62:63], s[12:13], 0, v[124:125]
	v_lshl_add_u64 v[62:63], v[62:63], 0, v[16:17]
	v_lshl_add_u64 v[106:107], v[62:63], 0, v[138:139]
	s_waitcnt vmcnt(6)
	v_pk_mul_f32 v[62:63], v[42:43], v[168:169] op_sel_hi:[1,0]
	global_store_dwordx4 v[106:107], v[86:89], off sc1
	s_waitcnt vmcnt(6)
	v_pk_fma_f32 v[64:65], v[42:43], v[164:165], v[62:63] op_sel:[0,0,1] op_sel_hi:[1,1,0] neg_lo:[0,0,1] neg_hi:[0,0,1]
	v_pk_fma_f32 v[42:43], v[42:43], v[164:165], v[62:63] op_sel:[0,0,1] op_sel_hi:[1,0,0]
	v_pk_mul_f32 v[62:63], v[44:45], v[168:169] op_sel:[0,1]
	v_cvt_pk_f16_f32 v42, v64, v43
	v_pk_fma_f32 v[74:75], v[44:45], v[164:165], v[62:63] op_sel:[0,1,1] op_sel_hi:[1,1,0] neg_lo:[0,0,1] neg_hi:[0,0,1]
	v_pk_fma_f32 v[44:45], v[44:45], v[164:165], v[62:63] op_sel:[0,1,1] op_sel_hi:[1,1,0]
	v_mov_b32_e32 v86, v171
	v_cvt_pk_f16_f32 v43, v74, v45
	v_pk_mul_f32 v[44:45], v[58:59], v[170:171] op_sel_hi:[1,0]
	v_mov_b32_e32 v88, v167
	v_pk_fma_f32 v[74:75], v[58:59], v[166:167], v[44:45] op_sel:[0,0,1] op_sel_hi:[1,1,0] neg_lo:[0,0,1] neg_hi:[0,0,1]
	v_pk_fma_f32 v[44:45], v[58:59], v[166:167], v[44:45] op_sel:[0,0,1] op_sel_hi:[1,0,0]
	v_pk_mul_f32 v[58:59], v[60:61], v[86:87] op_sel_hi:[1,0]
	v_cvt_pk_f16_f32 v44, v74, v45
	v_pk_fma_f32 v[108:109], v[60:61], v[88:89], v[58:59] op_sel:[0,0,1] op_sel_hi:[1,0,0] neg_lo:[0,0,1] neg_hi:[0,0,1]
	v_pk_fma_f32 v[58:59], v[60:61], v[88:89], v[58:59] op_sel:[0,0,1] op_sel_hi:[1,0,0]
	v_mfma_f32_16x16x32_f16 v[74:77], v[194:197], v[172:175], v[78:81]
	v_cvt_pk_f16_f32 v45, v108, v59
	global_store_dwordx4 v[126:127], v[42:45], off offset:2048 sc1
	v_pk_mul_f32 v[58:59], v[54:55], v[168:169] op_sel_hi:[1,0]
	v_mfma_f32_16x16x32_f16 v[22:25], v[180:183], v[176:179], v[22:25]
	v_fma_f32 v78, v54, v164, -v59
	v_fma_f32 v79, v55, v165, -v58
	v_pk_fma_f32 v[54:55], v[54:55], v[164:165], v[58:59] op_sel:[0,0,1] op_sel_hi:[1,0,0]
	v_mfma_f32_16x16x32_f16 v[42:45], v[198:201], v[172:175], v[82:85]
	v_cvt_pk_f16_f32 v54, v78, v55
	s_nop 1
	v_pk_mul_f32 v[82:83], v[56:57], v[168:169] op_sel:[0,1]
	v_mfma_f32_16x16x32_f16 v[30:33], v[194:197], v[176:179], v[30:33]
	v_fma_f32 v84, v56, v165, -v83
	v_fma_f32 v85, v57, v165, -v82
	v_pk_fma_f32 v[56:57], v[56:57], v[164:165], v[82:83] op_sel:[0,1,1] op_sel_hi:[1,1,0]
	s_nop 0
	v_cvt_pk_f16_f32 v55, v84, v57
	v_pk_mul_f32 v[56:57], v[50:51], v[170:171] op_sel_hi:[1,0]
	v_mfma_f32_16x16x32_f16 v[26:29], v[198:201], v[176:179], v[26:29]
	v_fma_f32 v82, v50, v166, -v57
	v_fma_f32 v83, v51, v167, -v56
	v_pk_fma_f32 v[50:51], v[50:51], v[166:167], v[56:57] op_sel:[0,0,1] op_sel_hi:[1,0,0]
	s_nop 0
	v_cvt_pk_f16_f32 v56, v82, v51
	v_pk_mul_f32 v[50:51], v[52:53], v[86:87] op_sel_hi:[1,0]
	v_mfma_f32_16x16x32_f16 v[82:85], v[184:187], v[176:179], v[102:105]
	v_fma_f32 v86, v52, v88, -v51
	v_fma_f32 v87, v53, v88, -v50
	v_pk_fma_f32 v[50:51], v[52:53], v[88:89], v[50:51] op_sel:[0,0,1] op_sel_hi:[1,0,0]
	s_nop 0
	v_cvt_pk_f16_f32 v57, v86, v51
	global_store_dwordx4 v[106:107], v[54:57], off offset:2048 sc1
	s_waitcnt vmcnt(7)
	v_pk_mul_f32 v[50:51], v[38:39], v[210:211] op_sel_hi:[1,0]
	v_mfma_f32_16x16x32_f16 v[70:73], v[140:143], v[202:205], v[70:73]
	v_mul_f32_e64 v56, v40, v211
	v_mul_f32_e64 v57, v41, v211
	s_waitcnt vmcnt(6)
	v_pk_fma_f32 v[52:53], v[38:39], v[4:5], v[50:51] op_sel:[0,0,1] op_sel_hi:[1,1,0] neg_lo:[0,0,1] neg_hi:[0,0,1]
	v_pk_fma_f32 v[38:39], v[38:39], v[4:5], v[50:51] op_sel:[0,0,1] op_sel_hi:[1,0,0]
	v_pk_fma_f32 v[86:87], v[40:41], v[4:5], v[56:57] op_sel:[0,1,1] op_sel_hi:[1,1,0] neg_lo:[0,0,1] neg_hi:[0,0,1]
	v_pk_fma_f32 v[40:41], v[40:41], v[4:5], v[56:57] op_sel:[0,1,1] op_sel_hi:[1,1,0]
	v_cvt_pk_f16_f32 v38, v52, v39
	v_cvt_pk_f16_f32 v39, v86, v41
	v_pk_mul_f32 v[40:41], v[66:67], v[212:213] op_sel_hi:[1,0]
	v_or_b32_e32 v54, 0x800, v118
	v_pk_fma_f32 v[56:57], v[66:67], v[6:7], v[40:41] op_sel:[0,0,1] op_sel_hi:[1,1,0] neg_lo:[0,0,1] neg_hi:[0,0,1]
	v_pk_fma_f32 v[40:41], v[66:67], v[6:7], v[40:41] op_sel:[0,0,1] op_sel_hi:[1,0,0]
	v_mov_b32_e32 v55, v119
	v_cvt_pk_f16_f32 v40, v56, v41
	v_mov_b32_e32 v56, v213
	v_pk_mul_f32 v[66:67], v[68:69], v[56:57] op_sel_hi:[1,0]
	v_mov_b32_e32 v86, v7
	v_pk_fma_f32 v[88:89], v[68:69], v[86:87], v[66:67] op_sel:[0,0,1] op_sel_hi:[1,0,0] neg_lo:[0,0,1] neg_hi:[0,0,1]
	v_pk_fma_f32 v[66:67], v[68:69], v[86:87], v[66:67] op_sel:[0,0,1] op_sel_hi:[1,0,0]
	v_lshlrev_b64 v[54:55], 1, v[54:55]
	v_cvt_pk_f16_f32 v41, v88, v67
	v_lshl_add_u64 v[66:67], s[10:11], 0, v[54:55]
	v_lshl_add_u64 v[66:67], v[66:67], 0, v[16:17]
	v_lshl_add_u64 v[66:67], v[66:67], 0, v[138:139]
	global_store_dwordx4 v[66:67], v[38:41], off sc1
	v_or_b32_e32 v118, 0xc00, v118
	v_mfma_f32_16x16x32_f16 v[46:49], v[148:151], v[202:205], v[46:49]
	v_mul_f32_e64 v38, v74, v210
	v_mul_f32_e64 v39, v75, v210
	v_pk_fma_f32 v[40:41], v[74:75], v[4:5], v[38:39] op_sel:[0,0,1] op_sel_hi:[1,1,0] neg_lo:[0,0,1] neg_hi:[0,0,1]
	v_pk_fma_f32 v[38:39], v[74:75], v[4:5], v[38:39] op_sel:[0,0,1] op_sel_hi:[1,0,0]
	v_mfma_f32_16x16x32_f16 v[58:61], v[172:175], v[202:205], v[90:93]
	v_cvt_pk_f16_f32 v38, v40, v39
	v_pk_mul_f32 v[40:41], v[76:77], v[210:211] op_sel:[0,1]
	s_nop 0
	v_pk_fma_f32 v[66:67], v[76:77], v[4:5], v[40:41] op_sel:[0,1,1] op_sel_hi:[1,1,0] neg_lo:[0,0,1] neg_hi:[0,0,1]
	v_pk_fma_f32 v[4:5], v[76:77], v[4:5], v[40:41] op_sel:[0,1,1] op_sel_hi:[1,1,0]
	v_mfma_f32_16x16x32_f16 v[34:37], v[176:179], v[202:205], v[34:37]
	v_cvt_pk_f16_f32 v39, v66, v5
	v_pk_mul_f32 v[4:5], v[42:43], v[212:213] op_sel_hi:[1,0]
	s_nop 0
	v_pk_fma_f32 v[40:41], v[42:43], v[6:7], v[4:5] op_sel:[0,0,1] op_sel_hi:[1,1,0] neg_lo:[0,0,1] neg_hi:[0,0,1]
	v_pk_fma_f32 v[4:5], v[42:43], v[6:7], v[4:5] op_sel:[0,0,1] op_sel_hi:[1,0,0]
	v_mfma_f32_16x16x32_f16 v[62:65], v[148:151], v[206:209], v[110:113]
	v_cvt_pk_f16_f32 v40, v40, v5
	v_pk_mul_f32 v[4:5], v[44:45], v[56:57] op_sel_hi:[1,0]
	s_nop 0
	v_pk_fma_f32 v[6:7], v[44:45], v[86:87], v[4:5] op_sel:[0,0,1] op_sel_hi:[1,0,0] neg_lo:[0,0,1] neg_hi:[0,0,1]
	v_pk_fma_f32 v[4:5], v[44:45], v[86:87], v[4:5] op_sel:[0,0,1] op_sel_hi:[1,0,0]
	v_mfma_f32_16x16x32_f16 v[78:81], v[172:175], v[206:209], v[94:97]
	v_cvt_pk_f16_f32 v41, v6, v5
	v_lshl_add_u64 v[4:5], s[12:13], 0, v[54:55]
	v_lshl_add_u64 v[4:5], v[4:5], 0, v[16:17]
	v_lshl_add_u64 v[4:5], v[4:5], 0, v[138:139]
	global_store_dwordx4 v[4:5], v[38:41], off sc1
	s_waitcnt vmcnt(7)
	v_pk_mul_f32 v[4:5], v[22:23], v[8:9] op_sel_hi:[1,0]
	v_mfma_f32_16x16x32_f16 v[50:53], v[176:179], v[206:209], v[98:101]
	s_waitcnt vmcnt(6)
	v_pk_fma_f32 v[6:7], v[22:23], v[0:1], v[4:5] op_sel:[0,0,1] op_sel_hi:[1,1,0] neg_lo:[0,0,1] neg_hi:[0,0,1]
	v_pk_fma_f32 v[4:5], v[22:23], v[0:1], v[4:5] op_sel:[0,0,1] op_sel_hi:[1,0,0]
	v_mov_b32_e32 v38, v3
	v_cvt_pk_f16_f32 v4, v6, v5
	v_pk_mul_f32 v[6:7], v[24:25], v[8:9] op_sel:[0,1]
	s_nop 0
	v_pk_fma_f32 v[22:23], v[24:25], v[0:1], v[6:7] op_sel:[0,1,1] op_sel_hi:[1,1,0] neg_lo:[0,0,1] neg_hi:[0,0,1]
	v_pk_fma_f32 v[6:7], v[24:25], v[0:1], v[6:7] op_sel:[0,1,1] op_sel_hi:[1,1,0]
	s_nop 0
	v_cvt_pk_f16_f32 v5, v22, v7
	v_pk_mul_f32 v[6:7], v[82:83], v[10:11] op_sel_hi:[1,0]
	s_nop 0
	v_pk_fma_f32 v[22:23], v[82:83], v[2:3], v[6:7] op_sel:[0,0,1] op_sel_hi:[1,1,0] neg_lo:[0,0,1] neg_hi:[0,0,1]
	v_pk_fma_f32 v[6:7], v[82:83], v[2:3], v[6:7] op_sel:[0,0,1] op_sel_hi:[1,0,0]
	s_nop 0
	v_cvt_pk_f16_f32 v6, v22, v7
	v_mov_b32_e32 v22, v11
	v_pk_mul_f32 v[24:25], v[84:85], v[22:23] op_sel_hi:[1,0]
	s_nop 0
	v_pk_fma_f32 v[40:41], v[84:85], v[38:39], v[24:25] op_sel:[0,0,1] op_sel_hi:[1,0,0] neg_lo:[0,0,1] neg_hi:[0,0,1]
	v_pk_fma_f32 v[24:25], v[84:85], v[38:39], v[24:25] op_sel:[0,0,1] op_sel_hi:[1,0,0]
	s_nop 0
	v_cvt_pk_f16_f32 v7, v40, v25
	v_lshlrev_b64 v[24:25], 1, v[118:119]
	v_lshl_add_u64 v[40:41], s[10:11], 0, v[24:25]
	v_lshl_add_u64 v[40:41], v[40:41], 0, v[16:17]
	v_lshl_add_u64 v[40:41], v[40:41], 0, v[138:139]
	global_store_dwordx4 v[40:41], v[4:7], off sc1
	s_nop 1
	v_pk_mul_f32 v[4:5], v[30:31], v[8:9] op_sel_hi:[1,0]
	s_nop 0
	v_pk_fma_f32 v[6:7], v[30:31], v[0:1], v[4:5] op_sel:[0,0,1] op_sel_hi:[1,1,0] neg_lo:[0,0,1] neg_hi:[0,0,1]
	v_pk_fma_f32 v[4:5], v[30:31], v[0:1], v[4:5] op_sel:[0,0,1] op_sel_hi:[1,0,0]
	s_nop 0
	v_cvt_pk_f16_f32 v4, v6, v5
	v_pk_mul_f32 v[6:7], v[32:33], v[8:9] op_sel:[0,1]
	s_nop 0
	v_pk_fma_f32 v[8:9], v[32:33], v[0:1], v[6:7] op_sel:[0,1,1] op_sel_hi:[1,1,0] neg_lo:[0,0,1] neg_hi:[0,0,1]
	v_pk_fma_f32 v[0:1], v[32:33], v[0:1], v[6:7] op_sel:[0,1,1] op_sel_hi:[1,1,0]
	s_nop 0
	v_cvt_pk_f16_f32 v5, v8, v1
	v_pk_mul_f32 v[0:1], v[26:27], v[10:11] op_sel_hi:[1,0]
	s_nop 0
	v_pk_fma_f32 v[6:7], v[26:27], v[2:3], v[0:1] op_sel:[0,0,1] op_sel_hi:[1,1,0] neg_lo:[0,0,1] neg_hi:[0,0,1]
	v_pk_fma_f32 v[0:1], v[26:27], v[2:3], v[0:1] op_sel:[0,0,1] op_sel_hi:[1,0,0]
	s_nop 0
	v_cvt_pk_f16_f32 v6, v6, v1
	v_pk_mul_f32 v[0:1], v[28:29], v[22:23] op_sel_hi:[1,0]
	s_nop 0
	v_pk_fma_f32 v[2:3], v[28:29], v[38:39], v[0:1] op_sel:[0,0,1] op_sel_hi:[1,0,0] neg_lo:[0,0,1] neg_hi:[0,0,1]
	v_pk_fma_f32 v[0:1], v[28:29], v[38:39], v[0:1] op_sel:[0,0,1] op_sel_hi:[1,0,0]
	v_cvt_pk_f16_f32 v3, v48, v49
	v_cvt_pk_f16_f32 v7, v2, v1
	v_lshl_add_u64 v[0:1], s[12:13], 0, v[24:25]
	v_lshl_add_u64 v[0:1], v[0:1], 0, v[16:17]
	v_lshl_add_u64 v[0:1], v[0:1], 0, v[138:139]
	global_store_dwordx4 v[0:1], v[4:7], off sc1
	v_lshlrev_b64 v[0:1], 18, v[18:19]
	v_lshlrev_b32_e32 v2, 7, v145
	v_lshl_add_u64 v[0:1], s[14:15], 0, v[0:1]
	v_and_b32_e32 v16, 0x3e000, v2
	v_lshl_add_u64 v[0:1], v[0:1], 0, v[16:17]
	v_lshlrev_b32_e32 v16, 4, v20
	v_lshl_add_u64 v[4:5], v[0:1], 0, v[16:17]
	v_lshlrev_b32_e32 v16, 12, v144
	v_cvt_pk_f16_f32 v2, v46, v47
	v_cvt_pk_f16_f32 v1, v72, v73
	v_cvt_pk_f16_f32 v0, v70, v71
	v_lshl_add_u64 v[4:5], v[4:5], 0, v[16:17]
	global_store_dwordx4 v[4:5], v[0:3], off sc1
	s_nop 1
	v_cvt_pk_f16_f32 v3, v36, v37
	v_cvt_pk_f16_f32 v2, v34, v35
	v_cvt_pk_f16_f32 v1, v60, v61
	v_cvt_pk_f16_f32 v0, v58, v59
	global_store_dwordx4 v[4:5], v[0:3], off offset:1024 sc1
	s_nop 1
	v_cvt_pk_f16_f32 v3, v64, v65
	v_cvt_pk_f16_f32 v2, v62, v63
	v_cvt_pk_f16_f32 v1, v14, v15
	v_cvt_pk_f16_f32 v0, v12, v13
	global_store_dwordx4 v[4:5], v[0:3], off offset:2048 sc1
	s_nop 1
	v_cvt_pk_f16_f32 v3, v52, v53
	v_cvt_pk_f16_f32 v2, v50, v51
	v_cvt_pk_f16_f32 v1, v80, v81
	v_cvt_pk_f16_f32 v0, v78, v79
	global_store_dwordx4 v[4:5], v[0:3], off offset:3072 sc1
	s_endpgm
	.p2align	8

	.text
	.p2alignl 8, 3212836864
	.fill 256, 4, 3212836864
